# adds P1 router-constant slices: 64 loads in flight instead of 4 drained groups of 16
# speedup vs baseline: 1.0049x; 1.0045x over previous
; __device__ __forceinline__ void p1_modulate(Frame& F, const Args& A) {
;     ...
;     if (F.vcu < 64 && F.wave == 0) { const int b = F.vcu >> 5, kq = F.vcu & 31, e = F.lane & 31, ks = F.lane >> 5; float s = 0.f;
; #pragma unroll 8
;         for (int i = 0; i < 32; ++i) { const int k = 64 * kq + 2 * i + ks; s = fmaf(MOD[b * 12288 + 3 * DM + k], A.in[I_WR][k * 32 + e], s); }
;         s += __shfl_xor(s, 32); if (F.lane < 32) WSP(float, WS_RC)[(b * 32 + kq) * 32 + e] = s; }
.LBB0_49:
	v_add_u32_e32 v24, -14, v6
	v_ashrrev_i32_e32 v25, 31, v24
	v_lshl_add_u64 v[24:25], v[24:25], 2, s[8:9]
	v_add_co_u32_e32 v174, vcc, 0x1000, v20
	s_nop 1
	v_addc_co_u32_e32 v175, vcc, 0, v21, vcc
	v_add_co_u32_e32 v176, vcc, 0x1000, v18
	s_nop 1
	v_addc_co_u32_e32 v177, vcc, 0, v19, vcc
	v_add_co_u32_e32 v178, vcc, 0x1000, v16
	s_nop 1
	v_addc_co_u32_e32 v179, vcc, 0, v17, vcc
	v_add_co_u32_e32 v180, vcc, 0x1000, v14
	s_nop 1
	v_addc_co_u32_e32 v181, vcc, 0, v15, vcc
	v_add_co_u32_e32 v182, vcc, 0x1000, v12
	s_nop 1
	v_addc_co_u32_e32 v183, vcc, 0, v13, vcc
	v_add_co_u32_e32 v184, vcc, 0x1000, v10
	s_nop 1
	v_addc_co_u32_e32 v185, vcc, 0, v11, vcc
	v_add_co_u32_e32 v186, vcc, 0x1000, v8
	s_nop 1
	v_addc_co_u32_e32 v187, vcc, 0, v9, vcc
	v_add_co_u32_e32 v188, vcc, 0x1000, v4
	s_nop 1
	v_addc_co_u32_e32 v189, vcc, 0, v5, vcc
	global_load_dword v110, v[24:25], off
	global_load_dword v111, v[20:21], off
	global_load_dword v112, v[24:25], off offset:8
	global_load_dword v113, v[18:19], off
	global_load_dword v114, v[24:25], off offset:16
	global_load_dword v115, v[16:17], off
	global_load_dword v116, v[24:25], off offset:24
	global_load_dword v117, v[14:15], off
	global_load_dword v118, v[24:25], off offset:32
	global_load_dword v119, v[12:13], off
	global_load_dword v120, v[24:25], off offset:40
	global_load_dword v121, v[10:11], off
	global_load_dword v122, v[24:25], off offset:48
	global_load_dword v123, v[8:9], off
	global_load_dword v124, v[24:25], off offset:56
	global_load_dword v125, v[4:5], off
	global_load_dword v126, v[24:25], off offset:64
	global_load_dword v127, v[20:21], off offset:2048
	global_load_dword v128, v[24:25], off offset:72
	global_load_dword v129, v[18:19], off offset:2048
	global_load_dword v130, v[24:25], off offset:80
	global_load_dword v131, v[16:17], off offset:2048
	global_load_dword v132, v[24:25], off offset:88
	global_load_dword v133, v[14:15], off offset:2048
	global_load_dword v134, v[24:25], off offset:96
	global_load_dword v135, v[12:13], off offset:2048
	global_load_dword v136, v[24:25], off offset:104
	global_load_dword v137, v[10:11], off offset:2048
	global_load_dword v138, v[24:25], off offset:112
	global_load_dword v139, v[8:9], off offset:2048
	global_load_dword v140, v[24:25], off offset:120
	global_load_dword v141, v[4:5], off offset:2048
	global_load_dword v142, v[24:25], off offset:128
	global_load_dword v143, v[174:175], off
	global_load_dword v144, v[24:25], off offset:136
	global_load_dword v145, v[176:177], off
	global_load_dword v146, v[24:25], off offset:144
	global_load_dword v147, v[178:179], off
	global_load_dword v148, v[24:25], off offset:152
	global_load_dword v149, v[180:181], off
	global_load_dword v150, v[24:25], off offset:160
	global_load_dword v151, v[182:183], off
	global_load_dword v152, v[24:25], off offset:168
	global_load_dword v153, v[184:185], off
	global_load_dword v154, v[24:25], off offset:176
	global_load_dword v155, v[186:187], off
	global_load_dword v156, v[24:25], off offset:184
	global_load_dword v157, v[188:189], off
	global_load_dword v158, v[24:25], off offset:192
	global_load_dword v159, v[174:175], off offset:2048
	global_load_dword v160, v[24:25], off offset:200
	global_load_dword v161, v[176:177], off offset:2048
	global_load_dword v162, v[24:25], off offset:208
	global_load_dword v163, v[178:179], off offset:2048
	global_load_dword v164, v[24:25], off offset:216
	global_load_dword v165, v[180:181], off offset:2048
	global_load_dword v166, v[24:25], off offset:224
	global_load_dword v167, v[182:183], off offset:2048
	global_load_dword v168, v[24:25], off offset:232
	global_load_dword v169, v[184:185], off offset:2048
	global_load_dword v170, v[24:25], off offset:240
	global_load_dword v171, v[186:187], off offset:2048
	global_load_dword v172, v[24:25], off offset:248
	global_load_dword v173, v[188:189], off offset:2048
	s_waitcnt vmcnt(62)
	v_fmac_f32_e32 v3, v110, v111
	s_waitcnt vmcnt(60)
	v_fmac_f32_e32 v3, v112, v113
	s_waitcnt vmcnt(58)
	v_fmac_f32_e32 v3, v114, v115
	s_waitcnt vmcnt(56)
	v_fmac_f32_e32 v3, v116, v117
	s_waitcnt vmcnt(54)
	v_fmac_f32_e32 v3, v118, v119
	s_waitcnt vmcnt(52)
	v_fmac_f32_e32 v3, v120, v121
	s_waitcnt vmcnt(50)
	v_fmac_f32_e32 v3, v122, v123
	s_waitcnt vmcnt(48)
	v_fmac_f32_e32 v3, v124, v125
	s_waitcnt vmcnt(46)
	v_fmac_f32_e32 v3, v126, v127
	s_waitcnt vmcnt(44)
	v_fmac_f32_e32 v3, v128, v129
	s_waitcnt vmcnt(42)
	v_fmac_f32_e32 v3, v130, v131
	s_waitcnt vmcnt(40)
	v_fmac_f32_e32 v3, v132, v133
	s_waitcnt vmcnt(38)
	v_fmac_f32_e32 v3, v134, v135
	s_waitcnt vmcnt(36)
	v_fmac_f32_e32 v3, v136, v137
	s_waitcnt vmcnt(34)
	v_fmac_f32_e32 v3, v138, v139
	s_waitcnt vmcnt(32)
	v_fmac_f32_e32 v3, v140, v141
	s_waitcnt vmcnt(30)
	v_fmac_f32_e32 v3, v142, v143
	s_waitcnt vmcnt(28)
	v_fmac_f32_e32 v3, v144, v145
	s_waitcnt vmcnt(26)
	v_fmac_f32_e32 v3, v146, v147
	s_waitcnt vmcnt(24)
	v_fmac_f32_e32 v3, v148, v149
	s_waitcnt vmcnt(22)
	v_fmac_f32_e32 v3, v150, v151
	s_waitcnt vmcnt(20)
	v_fmac_f32_e32 v3, v152, v153
	s_waitcnt vmcnt(18)
	v_fmac_f32_e32 v3, v154, v155
	s_waitcnt vmcnt(16)
	v_fmac_f32_e32 v3, v156, v157
	s_waitcnt vmcnt(14)
	v_fmac_f32_e32 v3, v158, v159
	s_waitcnt vmcnt(12)
	v_fmac_f32_e32 v3, v160, v161
	s_waitcnt vmcnt(10)
	v_fmac_f32_e32 v3, v162, v163
	s_waitcnt vmcnt(8)
	v_fmac_f32_e32 v3, v164, v165
	s_waitcnt vmcnt(6)
	v_fmac_f32_e32 v3, v166, v167
	s_waitcnt vmcnt(4)
	v_fmac_f32_e32 v3, v168, v169
	s_waitcnt vmcnt(2)
	v_fmac_f32_e32 v3, v170, v171
	s_waitcnt vmcnt(0)
	v_fmac_f32_e32 v3, v172, v173
	v_mbcnt_lo_u32_b32 v2, -1, 0
	v_mbcnt_hi_u32_b32 v2, -1, v2
	v_and_b32_e32 v5, 64, v2
	v_xor_b32_e32 v4, 32, v2
	v_add_u32_e32 v5, 64, v5
	v_cmp_lt_i32_e32 vcc, v4, v5
	s_nop 1
	v_cndmask_b32_e32 v2, v2, v4, vcc
	v_lshlrev_b32_e32 v2, 2, v2
	ds_bpermute_b32 v2, v2, v3
	v_cmp_gt_u32_e32 vcc, 32, v1
	s_and_saveexec_b64 s[4:5], vcc
	s_cbranch_execz .LBB0_52
	v_lshl_or_b32 v4, s90, 5, v22
	v_ashrrev_i32_e32 v5, 31, v4
	v_lshl_add_u64 v[4:5], v[4:5], 2, s[30:31]
	s_waitcnt lgkmcnt(0)
	v_add_f32_e32 v6, v3, v2
	v_add_co_u32_e32 v2, vcc, 0x180000, v4
	s_nop 1
	v_addc_co_u32_e32 v3, vcc, 0, v5, vcc
	global_store_dword v[2:3], v6, off
